# MoE GEMM1 epilogue hand-rewritten with packed f32 ops (v_pk_fma/mul/add), same op order and rounding, 40 percent fewer VALU instructions
# speedup vs baseline: 1.0113x; 1.0113x over previous
.LBB0_1485:
	s_lshl_b32 s1, s30, 7
	s_ashr_i32 s0, s30, 4
	s_and_b32 s1, s1, 0x780
	v_or_b32_e32 v170, s1, v184
	v_lshl_add_u32 v20, s28, 8, v182
	s_mov_b32 s98, 0x3a800000
	s_mov_b32 s99, 0x3fd9db23
	s_mov_b32 s100, 0xbfb8aa3b
	s_mov_b32 s101, 4.0
	v_ashrrev_i32_e32 v21, 31, v20
	v_mov_b32_e32 v12, v170
	v_mov_b32_e32 v13, 0
	v_mov_b32_e32 v15, 0
	v_mov_b32_e32 v16, 1.0
	v_mov_b32_e32 v17, 1.0
	v_lshlrev_b64 v[18:19], 11, v[20:21]
	v_lshl_add_u64 v[18:19], s[14:15], 0, v[18:19]
	v_lshl_add_u64 v[18:19], v[18:19], 0, v[12:13]
	v_pk_fma_f32 v[158:159], v[158:159], s[98:99], v[224:225] op_sel_hi:[1,0,1]
	v_pk_fma_f32 v[160:161], v[160:161], s[98:99], v[226:227] op_sel_hi:[1,0,1]
	v_pk_fma_f32 v[154:155], v[154:155], s[98:99], v[228:229] op_sel_hi:[1,0,1]
	v_pk_fma_f32 v[156:157], v[156:157], s[98:99], v[230:231] op_sel_hi:[1,0,1]
	v_pk_fma_f32 v[150:151], v[150:151], s[98:99], v[232:233] op_sel_hi:[1,0,1]
	v_pk_fma_f32 v[152:153], v[152:153], s[98:99], v[234:235] op_sel_hi:[1,0,1]
	v_pk_fma_f32 v[146:147], v[146:147], s[98:99], v[236:237] op_sel_hi:[1,0,1]
	v_pk_fma_f32 v[148:149], v[148:149], s[98:99], v[238:239] op_sel_hi:[1,0,1]
	v_min_f32_e32 v158, 0x40e00000, v158
	v_min_f32_e32 v159, 0x40e00000, v159
	v_min_f32_e32 v160, 0x40e00000, v160
	v_min_f32_e32 v161, 0x40e00000, v161
	v_min_f32_e32 v154, 0x40e00000, v154
	v_min_f32_e32 v155, 0x40e00000, v155
	v_min_f32_e32 v156, 0x40e00000, v156
	v_min_f32_e32 v157, 0x40e00000, v157
	v_med3_f32 v150, v150, s59, v189
	v_med3_f32 v151, v151, s59, v189
	v_med3_f32 v152, v152, s59, v189
	v_med3_f32 v153, v153, s59, v189
	v_med3_f32 v146, v146, s59, v189
	v_med3_f32 v147, v147, s59, v189
	v_med3_f32 v148, v148, s59, v189
	v_med3_f32 v149, v149, s59, v189
	v_pk_mul_f32 v[2:3], v[158:159], s[98:99] op_sel:[0,1]
	v_pk_mul_f32 v[4:5], v[160:161], s[98:99] op_sel:[0,1]
	v_pk_mul_f32 v[6:7], v[154:155], s[98:99] op_sel:[0,1]
	v_pk_mul_f32 v[8:9], v[156:157], s[98:99] op_sel:[0,1]
	v_pk_mul_f32 v[2:3], v[2:3], s[100:101] op_sel_hi:[1,0]
	v_pk_mul_f32 v[4:5], v[4:5], s[100:101] op_sel_hi:[1,0]
	v_pk_mul_f32 v[6:7], v[6:7], s[100:101] op_sel_hi:[1,0]
	v_pk_mul_f32 v[8:9], v[8:9], s[100:101] op_sel_hi:[1,0]
	v_exp_f32_e32 v2, v2
	v_exp_f32_e32 v3, v3
	v_exp_f32_e32 v4, v4
	v_exp_f32_e32 v5, v5
	v_exp_f32_e32 v6, v6
	v_exp_f32_e32 v7, v7
	v_exp_f32_e32 v8, v8
	v_exp_f32_e32 v9, v9
	v_pk_add_f32 v[150:151], v[150:151], v[16:17]
	v_pk_add_f32 v[152:153], v[152:153], v[16:17]
	v_pk_add_f32 v[146:147], v[146:147], v[16:17]
	v_pk_add_f32 v[148:149], v[148:149], v[16:17]
	v_pk_add_f32 v[2:3], v[2:3], v[16:17]
	v_pk_add_f32 v[4:5], v[4:5], v[16:17]
	v_pk_add_f32 v[6:7], v[6:7], v[16:17]
	v_pk_add_f32 v[8:9], v[8:9], v[16:17]
	v_pk_mul_f32 v[158:159], v[158:159], v[150:151]
	v_pk_mul_f32 v[160:161], v[160:161], v[152:153]
	v_pk_mul_f32 v[154:155], v[154:155], v[146:147]
	v_pk_mul_f32 v[156:157], v[156:157], v[148:149]
	v_rcp_f32_e32 v2, v2
	v_rcp_f32_e32 v3, v3
	v_rcp_f32_e32 v4, v4
	v_rcp_f32_e32 v5, v5
	v_rcp_f32_e32 v6, v6
	v_rcp_f32_e32 v7, v7
	v_rcp_f32_e32 v8, v8
	v_rcp_f32_e32 v9, v9
	s_nop 1
	v_pk_mul_f32 v[158:159], v[158:159], v[2:3]
	v_pk_mul_f32 v[160:161], v[160:161], v[4:5]
	v_pk_mul_f32 v[154:155], v[154:155], v[6:7]
	v_pk_mul_f32 v[156:157], v[156:157], v[8:9]
	v_pk_mul_f32 v[158:159], v[158:159], s[100:101] op_sel:[0,1]
	v_pk_mul_f32 v[160:161], v[160:161], s[100:101] op_sel:[0,1]
	v_pk_mul_f32 v[154:155], v[154:155], s[100:101] op_sel:[0,1]
	v_pk_mul_f32 v[156:157], v[156:157], s[100:101] op_sel:[0,1]
	v_cvt_pk_fp8_f32 v22, v158, v159
	v_cvt_pk_fp8_f32 v23, v154, v155
	v_cvt_pk_fp8_f32 v22, v160, v161 op_sel:[0,0,1]
	v_cvt_pk_fp8_f32 v23, v156, v157 op_sel:[0,0,1]
	global_store_dwordx2 v[18:19], v[22:23], off
	v_pk_fma_f32 v[142:143], v[142:143], s[98:99], v[224:225] op_sel_hi:[1,0,1]
	v_pk_fma_f32 v[144:145], v[144:145], s[98:99], v[226:227] op_sel_hi:[1,0,1]
	v_pk_fma_f32 v[138:139], v[138:139], s[98:99], v[228:229] op_sel_hi:[1,0,1]
	v_pk_fma_f32 v[140:141], v[140:141], s[98:99], v[230:231] op_sel_hi:[1,0,1]
	v_pk_fma_f32 v[134:135], v[134:135], s[98:99], v[232:233] op_sel_hi:[1,0,1]
	v_pk_fma_f32 v[136:137], v[136:137], s[98:99], v[234:235] op_sel_hi:[1,0,1]
	v_pk_fma_f32 v[130:131], v[130:131], s[98:99], v[236:237] op_sel_hi:[1,0,1]
	v_pk_fma_f32 v[132:133], v[132:133], s[98:99], v[238:239] op_sel_hi:[1,0,1]
	v_min_f32_e32 v142, 0x40e00000, v142
	v_min_f32_e32 v143, 0x40e00000, v143
	v_min_f32_e32 v144, 0x40e00000, v144
	v_min_f32_e32 v145, 0x40e00000, v145
	v_min_f32_e32 v138, 0x40e00000, v138
	v_min_f32_e32 v139, 0x40e00000, v139
	v_min_f32_e32 v140, 0x40e00000, v140
	v_min_f32_e32 v141, 0x40e00000, v141
	v_med3_f32 v134, v134, s59, v189
	v_med3_f32 v135, v135, s59, v189
	v_med3_f32 v136, v136, s59, v189
	v_med3_f32 v137, v137, s59, v189
	v_med3_f32 v130, v130, s59, v189
	v_med3_f32 v131, v131, s59, v189
	v_med3_f32 v132, v132, s59, v189
	v_med3_f32 v133, v133, s59, v189
	v_pk_mul_f32 v[2:3], v[142:143], s[98:99] op_sel:[0,1]
	v_pk_mul_f32 v[4:5], v[144:145], s[98:99] op_sel:[0,1]
	v_pk_mul_f32 v[6:7], v[138:139], s[98:99] op_sel:[0,1]
	v_pk_mul_f32 v[8:9], v[140:141], s[98:99] op_sel:[0,1]
	v_pk_mul_f32 v[2:3], v[2:3], s[100:101] op_sel_hi:[1,0]
	v_pk_mul_f32 v[4:5], v[4:5], s[100:101] op_sel_hi:[1,0]
	v_pk_mul_f32 v[6:7], v[6:7], s[100:101] op_sel_hi:[1,0]
	v_pk_mul_f32 v[8:9], v[8:9], s[100:101] op_sel_hi:[1,0]
	v_exp_f32_e32 v2, v2
	v_exp_f32_e32 v3, v3
	v_exp_f32_e32 v4, v4
	v_exp_f32_e32 v5, v5
	v_exp_f32_e32 v6, v6
	v_exp_f32_e32 v7, v7
	v_exp_f32_e32 v8, v8
	v_exp_f32_e32 v9, v9
	v_pk_add_f32 v[134:135], v[134:135], v[16:17]
	v_pk_add_f32 v[136:137], v[136:137], v[16:17]
	v_pk_add_f32 v[130:131], v[130:131], v[16:17]
	v_pk_add_f32 v[132:133], v[132:133], v[16:17]
	v_pk_add_f32 v[2:3], v[2:3], v[16:17]
	v_pk_add_f32 v[4:5], v[4:5], v[16:17]
	v_pk_add_f32 v[6:7], v[6:7], v[16:17]
	v_pk_add_f32 v[8:9], v[8:9], v[16:17]
	v_pk_mul_f32 v[142:143], v[142:143], v[134:135]
	v_pk_mul_f32 v[144:145], v[144:145], v[136:137]
	v_pk_mul_f32 v[138:139], v[138:139], v[130:131]
	v_pk_mul_f32 v[140:141], v[140:141], v[132:133]
	v_rcp_f32_e32 v2, v2
	v_rcp_f32_e32 v3, v3
	v_rcp_f32_e32 v4, v4
	v_rcp_f32_e32 v5, v5
	v_rcp_f32_e32 v6, v6
	v_rcp_f32_e32 v7, v7
	v_rcp_f32_e32 v8, v8
	v_rcp_f32_e32 v9, v9
	v_mov_b32_e32 v14, 0x8000
	v_lshl_add_u64 v[20:21], v[18:19], 0, v[14:15]
	v_pk_mul_f32 v[142:143], v[142:143], v[2:3]
	v_pk_mul_f32 v[144:145], v[144:145], v[4:5]
	v_pk_mul_f32 v[138:139], v[138:139], v[6:7]
	v_pk_mul_f32 v[140:141], v[140:141], v[8:9]
	v_pk_mul_f32 v[142:143], v[142:143], s[100:101] op_sel:[0,1]
	v_pk_mul_f32 v[144:145], v[144:145], s[100:101] op_sel:[0,1]
	v_pk_mul_f32 v[138:139], v[138:139], s[100:101] op_sel:[0,1]
	v_pk_mul_f32 v[140:141], v[140:141], s[100:101] op_sel:[0,1]
	v_cvt_pk_fp8_f32 v22, v142, v143
	v_cvt_pk_fp8_f32 v23, v138, v139
	v_cvt_pk_fp8_f32 v22, v144, v145 op_sel:[0,0,1]
	v_cvt_pk_fp8_f32 v23, v140, v141 op_sel:[0,0,1]
	global_store_dwordx2 v[20:21], v[22:23], off
	v_pk_fma_f32 v[126:127], v[126:127], s[98:99], v[224:225] op_sel_hi:[1,0,1]
	v_pk_fma_f32 v[128:129], v[128:129], s[98:99], v[226:227] op_sel_hi:[1,0,1]
	v_pk_fma_f32 v[122:123], v[122:123], s[98:99], v[228:229] op_sel_hi:[1,0,1]
	v_pk_fma_f32 v[124:125], v[124:125], s[98:99], v[230:231] op_sel_hi:[1,0,1]
	v_pk_fma_f32 v[118:119], v[118:119], s[98:99], v[232:233] op_sel_hi:[1,0,1]
	v_pk_fma_f32 v[120:121], v[120:121], s[98:99], v[234:235] op_sel_hi:[1,0,1]
	v_pk_fma_f32 v[114:115], v[114:115], s[98:99], v[236:237] op_sel_hi:[1,0,1]
	v_pk_fma_f32 v[116:117], v[116:117], s[98:99], v[238:239] op_sel_hi:[1,0,1]
	v_min_f32_e32 v126, 0x40e00000, v126
	v_min_f32_e32 v127, 0x40e00000, v127
	v_min_f32_e32 v128, 0x40e00000, v128
	v_min_f32_e32 v129, 0x40e00000, v129
	v_min_f32_e32 v122, 0x40e00000, v122
	v_min_f32_e32 v123, 0x40e00000, v123
	v_min_f32_e32 v124, 0x40e00000, v124
	v_min_f32_e32 v125, 0x40e00000, v125
	v_med3_f32 v118, v118, s59, v189
	v_med3_f32 v119, v119, s59, v189
	v_med3_f32 v120, v120, s59, v189
	v_med3_f32 v121, v121, s59, v189
	v_med3_f32 v114, v114, s59, v189
	v_med3_f32 v115, v115, s59, v189
	v_med3_f32 v116, v116, s59, v189
	v_med3_f32 v117, v117, s59, v189
	v_pk_mul_f32 v[2:3], v[126:127], s[98:99] op_sel:[0,1]
	v_pk_mul_f32 v[4:5], v[128:129], s[98:99] op_sel:[0,1]
	v_pk_mul_f32 v[6:7], v[122:123], s[98:99] op_sel:[0,1]
	v_pk_mul_f32 v[8:9], v[124:125], s[98:99] op_sel:[0,1]
	v_pk_mul_f32 v[2:3], v[2:3], s[100:101] op_sel_hi:[1,0]
	v_pk_mul_f32 v[4:5], v[4:5], s[100:101] op_sel_hi:[1,0]
	v_pk_mul_f32 v[6:7], v[6:7], s[100:101] op_sel_hi:[1,0]
	v_pk_mul_f32 v[8:9], v[8:9], s[100:101] op_sel_hi:[1,0]
	v_exp_f32_e32 v2, v2
	v_exp_f32_e32 v3, v3
	v_exp_f32_e32 v4, v4
	v_exp_f32_e32 v5, v5
	v_exp_f32_e32 v6, v6
	v_exp_f32_e32 v7, v7
	v_exp_f32_e32 v8, v8
	v_exp_f32_e32 v9, v9
	v_pk_add_f32 v[118:119], v[118:119], v[16:17]
	v_pk_add_f32 v[120:121], v[120:121], v[16:17]
	v_pk_add_f32 v[114:115], v[114:115], v[16:17]
	v_pk_add_f32 v[116:117], v[116:117], v[16:17]
	v_pk_add_f32 v[2:3], v[2:3], v[16:17]
	v_pk_add_f32 v[4:5], v[4:5], v[16:17]
	v_pk_add_f32 v[6:7], v[6:7], v[16:17]
	v_pk_add_f32 v[8:9], v[8:9], v[16:17]
	v_pk_mul_f32 v[126:127], v[126:127], v[118:119]
	v_pk_mul_f32 v[128:129], v[128:129], v[120:121]
	v_pk_mul_f32 v[122:123], v[122:123], v[114:115]
	v_pk_mul_f32 v[124:125], v[124:125], v[116:117]
	v_rcp_f32_e32 v2, v2
	v_rcp_f32_e32 v3, v3
	v_rcp_f32_e32 v4, v4
	v_rcp_f32_e32 v5, v5
	v_rcp_f32_e32 v6, v6
	v_rcp_f32_e32 v7, v7
	v_rcp_f32_e32 v8, v8
	v_rcp_f32_e32 v9, v9
	v_mov_b32_e32 v14, 0x10000
	v_lshl_add_u64 v[20:21], v[18:19], 0, v[14:15]
	v_pk_mul_f32 v[126:127], v[126:127], v[2:3]
	v_pk_mul_f32 v[128:129], v[128:129], v[4:5]
	v_pk_mul_f32 v[122:123], v[122:123], v[6:7]
	v_pk_mul_f32 v[124:125], v[124:125], v[8:9]
	v_pk_mul_f32 v[126:127], v[126:127], s[100:101] op_sel:[0,1]
	v_pk_mul_f32 v[128:129], v[128:129], s[100:101] op_sel:[0,1]
	v_pk_mul_f32 v[122:123], v[122:123], s[100:101] op_sel:[0,1]
	v_pk_mul_f32 v[124:125], v[124:125], s[100:101] op_sel:[0,1]
	v_cvt_pk_fp8_f32 v22, v126, v127
	v_cvt_pk_fp8_f32 v23, v122, v123
	v_cvt_pk_fp8_f32 v22, v128, v129 op_sel:[0,0,1]
	v_cvt_pk_fp8_f32 v23, v124, v125 op_sel:[0,0,1]
	global_store_dwordx2 v[20:21], v[22:23], off
	v_pk_fma_f32 v[110:111], v[110:111], s[98:99], v[224:225] op_sel_hi:[1,0,1]
	v_pk_fma_f32 v[112:113], v[112:113], s[98:99], v[226:227] op_sel_hi:[1,0,1]
	v_pk_fma_f32 v[106:107], v[106:107], s[98:99], v[228:229] op_sel_hi:[1,0,1]
	v_pk_fma_f32 v[108:109], v[108:109], s[98:99], v[230:231] op_sel_hi:[1,0,1]
	v_pk_fma_f32 v[102:103], v[102:103], s[98:99], v[232:233] op_sel_hi:[1,0,1]
	v_pk_fma_f32 v[104:105], v[104:105], s[98:99], v[234:235] op_sel_hi:[1,0,1]
	v_pk_fma_f32 v[98:99], v[98:99], s[98:99], v[236:237] op_sel_hi:[1,0,1]
	v_pk_fma_f32 v[100:101], v[100:101], s[98:99], v[238:239] op_sel_hi:[1,0,1]
	v_min_f32_e32 v110, 0x40e00000, v110
	v_min_f32_e32 v111, 0x40e00000, v111
	v_min_f32_e32 v112, 0x40e00000, v112
	v_min_f32_e32 v113, 0x40e00000, v113
	v_min_f32_e32 v106, 0x40e00000, v106
	v_min_f32_e32 v107, 0x40e00000, v107
	v_min_f32_e32 v108, 0x40e00000, v108
	v_min_f32_e32 v109, 0x40e00000, v109
	v_med3_f32 v102, v102, s59, v189
	v_med3_f32 v103, v103, s59, v189
	v_med3_f32 v104, v104, s59, v189
	v_med3_f32 v105, v105, s59, v189
	v_med3_f32 v98, v98, s59, v189
	v_med3_f32 v99, v99, s59, v189
	v_med3_f32 v100, v100, s59, v189
	v_med3_f32 v101, v101, s59, v189
	v_pk_mul_f32 v[2:3], v[110:111], s[98:99] op_sel:[0,1]
	v_pk_mul_f32 v[4:5], v[112:113], s[98:99] op_sel:[0,1]
	v_pk_mul_f32 v[6:7], v[106:107], s[98:99] op_sel:[0,1]
	v_pk_mul_f32 v[8:9], v[108:109], s[98:99] op_sel:[0,1]
	v_pk_mul_f32 v[2:3], v[2:3], s[100:101] op_sel_hi:[1,0]
	v_pk_mul_f32 v[4:5], v[4:5], s[100:101] op_sel_hi:[1,0]
	v_pk_mul_f32 v[6:7], v[6:7], s[100:101] op_sel_hi:[1,0]
	v_pk_mul_f32 v[8:9], v[8:9], s[100:101] op_sel_hi:[1,0]
	v_exp_f32_e32 v2, v2
	v_exp_f32_e32 v3, v3
	v_exp_f32_e32 v4, v4
	v_exp_f32_e32 v5, v5
	v_exp_f32_e32 v6, v6
	v_exp_f32_e32 v7, v7
	v_exp_f32_e32 v8, v8
	v_exp_f32_e32 v9, v9
	v_pk_add_f32 v[102:103], v[102:103], v[16:17]
	v_pk_add_f32 v[104:105], v[104:105], v[16:17]
	v_pk_add_f32 v[98:99], v[98:99], v[16:17]
	v_pk_add_f32 v[100:101], v[100:101], v[16:17]
	v_pk_add_f32 v[2:3], v[2:3], v[16:17]
	v_pk_add_f32 v[4:5], v[4:5], v[16:17]
	v_pk_add_f32 v[6:7], v[6:7], v[16:17]
	v_pk_add_f32 v[8:9], v[8:9], v[16:17]
	v_pk_mul_f32 v[110:111], v[110:111], v[102:103]
	v_pk_mul_f32 v[112:113], v[112:113], v[104:105]
	v_pk_mul_f32 v[106:107], v[106:107], v[98:99]
	v_pk_mul_f32 v[108:109], v[108:109], v[100:101]
	v_rcp_f32_e32 v2, v2
	v_rcp_f32_e32 v3, v3
	v_rcp_f32_e32 v4, v4
	v_rcp_f32_e32 v5, v5
	v_rcp_f32_e32 v6, v6
	v_rcp_f32_e32 v7, v7
	v_rcp_f32_e32 v8, v8
	v_rcp_f32_e32 v9, v9
	v_mov_b32_e32 v14, 0x18000
	v_lshl_add_u64 v[20:21], v[18:19], 0, v[14:15]
	v_pk_mul_f32 v[110:111], v[110:111], v[2:3]
	v_pk_mul_f32 v[112:113], v[112:113], v[4:5]
	v_pk_mul_f32 v[106:107], v[106:107], v[6:7]
	v_pk_mul_f32 v[108:109], v[108:109], v[8:9]
	v_pk_mul_f32 v[110:111], v[110:111], s[100:101] op_sel:[0,1]
	v_pk_mul_f32 v[112:113], v[112:113], s[100:101] op_sel:[0,1]
	v_pk_mul_f32 v[106:107], v[106:107], s[100:101] op_sel:[0,1]
	v_pk_mul_f32 v[108:109], v[108:109], s[100:101] op_sel:[0,1]
	v_cvt_pk_fp8_f32 v22, v110, v111
	v_cvt_pk_fp8_f32 v23, v106, v107
	v_cvt_pk_fp8_f32 v22, v112, v113 op_sel:[0,0,1]
	v_cvt_pk_fp8_f32 v23, v108, v109 op_sel:[0,0,1]
	global_store_dwordx2 v[20:21], v[22:23], off
	v_pk_fma_f32 v[94:95], v[94:95], s[98:99], v[224:225] op_sel_hi:[1,0,1]
	v_pk_fma_f32 v[96:97], v[96:97], s[98:99], v[226:227] op_sel_hi:[1,0,1]
	v_pk_fma_f32 v[90:91], v[90:91], s[98:99], v[228:229] op_sel_hi:[1,0,1]
	v_pk_fma_f32 v[92:93], v[92:93], s[98:99], v[230:231] op_sel_hi:[1,0,1]
	v_pk_fma_f32 v[86:87], v[86:87], s[98:99], v[232:233] op_sel_hi:[1,0,1]
	v_pk_fma_f32 v[88:89], v[88:89], s[98:99], v[234:235] op_sel_hi:[1,0,1]
	v_pk_fma_f32 v[82:83], v[82:83], s[98:99], v[236:237] op_sel_hi:[1,0,1]
	v_pk_fma_f32 v[84:85], v[84:85], s[98:99], v[238:239] op_sel_hi:[1,0,1]
	v_min_f32_e32 v94, 0x40e00000, v94
	v_min_f32_e32 v95, 0x40e00000, v95
	v_min_f32_e32 v96, 0x40e00000, v96
	v_min_f32_e32 v97, 0x40e00000, v97
	v_min_f32_e32 v90, 0x40e00000, v90
	v_min_f32_e32 v91, 0x40e00000, v91
	v_min_f32_e32 v92, 0x40e00000, v92
	v_min_f32_e32 v93, 0x40e00000, v93
	v_med3_f32 v86, v86, s59, v189
	v_med3_f32 v87, v87, s59, v189
	v_med3_f32 v88, v88, s59, v189
	v_med3_f32 v89, v89, s59, v189
	v_med3_f32 v82, v82, s59, v189
	v_med3_f32 v83, v83, s59, v189
	v_med3_f32 v84, v84, s59, v189
	v_med3_f32 v85, v85, s59, v189
	v_pk_mul_f32 v[2:3], v[94:95], s[98:99] op_sel:[0,1]
	v_pk_mul_f32 v[4:5], v[96:97], s[98:99] op_sel:[0,1]
	v_pk_mul_f32 v[6:7], v[90:91], s[98:99] op_sel:[0,1]
	v_pk_mul_f32 v[8:9], v[92:93], s[98:99] op_sel:[0,1]
	v_pk_mul_f32 v[2:3], v[2:3], s[100:101] op_sel_hi:[1,0]
	v_pk_mul_f32 v[4:5], v[4:5], s[100:101] op_sel_hi:[1,0]
	v_pk_mul_f32 v[6:7], v[6:7], s[100:101] op_sel_hi:[1,0]
	v_pk_mul_f32 v[8:9], v[8:9], s[100:101] op_sel_hi:[1,0]
	v_exp_f32_e32 v2, v2
	v_exp_f32_e32 v3, v3
	v_exp_f32_e32 v4, v4
	v_exp_f32_e32 v5, v5
	v_exp_f32_e32 v6, v6
	v_exp_f32_e32 v7, v7
	v_exp_f32_e32 v8, v8
	v_exp_f32_e32 v9, v9
	v_pk_add_f32 v[86:87], v[86:87], v[16:17]
	v_pk_add_f32 v[88:89], v[88:89], v[16:17]
	v_pk_add_f32 v[82:83], v[82:83], v[16:17]
	v_pk_add_f32 v[84:85], v[84:85], v[16:17]
	v_pk_add_f32 v[2:3], v[2:3], v[16:17]
	v_pk_add_f32 v[4:5], v[4:5], v[16:17]
	v_pk_add_f32 v[6:7], v[6:7], v[16:17]
	v_pk_add_f32 v[8:9], v[8:9], v[16:17]
	v_pk_mul_f32 v[94:95], v[94:95], v[86:87]
	v_pk_mul_f32 v[96:97], v[96:97], v[88:89]
	v_pk_mul_f32 v[90:91], v[90:91], v[82:83]
	v_pk_mul_f32 v[92:93], v[92:93], v[84:85]
	v_rcp_f32_e32 v2, v2
	v_rcp_f32_e32 v3, v3
	v_rcp_f32_e32 v4, v4
	v_rcp_f32_e32 v5, v5
	v_rcp_f32_e32 v6, v6
	v_rcp_f32_e32 v7, v7
	v_rcp_f32_e32 v8, v8
	v_rcp_f32_e32 v9, v9
	v_mov_b32_e32 v14, 0x40000
	v_lshl_add_u64 v[20:21], v[18:19], 0, v[14:15]
	v_pk_mul_f32 v[94:95], v[94:95], v[2:3]
	v_pk_mul_f32 v[96:97], v[96:97], v[4:5]
	v_pk_mul_f32 v[90:91], v[90:91], v[6:7]
	v_pk_mul_f32 v[92:93], v[92:93], v[8:9]
	v_pk_mul_f32 v[94:95], v[94:95], s[100:101] op_sel:[0,1]
	v_pk_mul_f32 v[96:97], v[96:97], s[100:101] op_sel:[0,1]
	v_pk_mul_f32 v[90:91], v[90:91], s[100:101] op_sel:[0,1]
	v_pk_mul_f32 v[92:93], v[92:93], s[100:101] op_sel:[0,1]
	v_cvt_pk_fp8_f32 v22, v94, v95
	v_cvt_pk_fp8_f32 v23, v90, v91
	v_cvt_pk_fp8_f32 v22, v96, v97 op_sel:[0,0,1]
	v_cvt_pk_fp8_f32 v23, v92, v93 op_sel:[0,0,1]
	global_store_dwordx2 v[20:21], v[22:23], off
	v_pk_fma_f32 v[78:79], v[78:79], s[98:99], v[224:225] op_sel_hi:[1,0,1]
	v_pk_fma_f32 v[80:81], v[80:81], s[98:99], v[226:227] op_sel_hi:[1,0,1]
	v_pk_fma_f32 v[74:75], v[74:75], s[98:99], v[228:229] op_sel_hi:[1,0,1]
	v_pk_fma_f32 v[76:77], v[76:77], s[98:99], v[230:231] op_sel_hi:[1,0,1]
	v_pk_fma_f32 v[70:71], v[70:71], s[98:99], v[232:233] op_sel_hi:[1,0,1]
	v_pk_fma_f32 v[72:73], v[72:73], s[98:99], v[234:235] op_sel_hi:[1,0,1]
	v_pk_fma_f32 v[66:67], v[66:67], s[98:99], v[236:237] op_sel_hi:[1,0,1]
	v_pk_fma_f32 v[68:69], v[68:69], s[98:99], v[238:239] op_sel_hi:[1,0,1]
	v_min_f32_e32 v78, 0x40e00000, v78
	v_min_f32_e32 v79, 0x40e00000, v79
	v_min_f32_e32 v80, 0x40e00000, v80
	v_min_f32_e32 v81, 0x40e00000, v81
	v_min_f32_e32 v74, 0x40e00000, v74
	v_min_f32_e32 v75, 0x40e00000, v75
	v_min_f32_e32 v76, 0x40e00000, v76
	v_min_f32_e32 v77, 0x40e00000, v77
	v_med3_f32 v70, v70, s59, v189
	v_med3_f32 v71, v71, s59, v189
	v_med3_f32 v72, v72, s59, v189
	v_med3_f32 v73, v73, s59, v189
	v_med3_f32 v66, v66, s59, v189
	v_med3_f32 v67, v67, s59, v189
	v_med3_f32 v68, v68, s59, v189
	v_med3_f32 v69, v69, s59, v189
	v_pk_mul_f32 v[2:3], v[78:79], s[98:99] op_sel:[0,1]
	v_pk_mul_f32 v[4:5], v[80:81], s[98:99] op_sel:[0,1]
	v_pk_mul_f32 v[6:7], v[74:75], s[98:99] op_sel:[0,1]
	v_pk_mul_f32 v[8:9], v[76:77], s[98:99] op_sel:[0,1]
	v_pk_mul_f32 v[2:3], v[2:3], s[100:101] op_sel_hi:[1,0]
	v_pk_mul_f32 v[4:5], v[4:5], s[100:101] op_sel_hi:[1,0]
	v_pk_mul_f32 v[6:7], v[6:7], s[100:101] op_sel_hi:[1,0]
	v_pk_mul_f32 v[8:9], v[8:9], s[100:101] op_sel_hi:[1,0]
	v_exp_f32_e32 v2, v2
	v_exp_f32_e32 v3, v3
	v_exp_f32_e32 v4, v4
	v_exp_f32_e32 v5, v5
	v_exp_f32_e32 v6, v6
	v_exp_f32_e32 v7, v7
	v_exp_f32_e32 v8, v8
	v_exp_f32_e32 v9, v9
	v_pk_add_f32 v[70:71], v[70:71], v[16:17]
	v_pk_add_f32 v[72:73], v[72:73], v[16:17]
	v_pk_add_f32 v[66:67], v[66:67], v[16:17]
	v_pk_add_f32 v[68:69], v[68:69], v[16:17]
	v_pk_add_f32 v[2:3], v[2:3], v[16:17]
	v_pk_add_f32 v[4:5], v[4:5], v[16:17]
	v_pk_add_f32 v[6:7], v[6:7], v[16:17]
	v_pk_add_f32 v[8:9], v[8:9], v[16:17]
	v_pk_mul_f32 v[78:79], v[78:79], v[70:71]
	v_pk_mul_f32 v[80:81], v[80:81], v[72:73]
	v_pk_mul_f32 v[74:75], v[74:75], v[66:67]
	v_pk_mul_f32 v[76:77], v[76:77], v[68:69]
	v_rcp_f32_e32 v2, v2
	v_rcp_f32_e32 v3, v3
	v_rcp_f32_e32 v4, v4
	v_rcp_f32_e32 v5, v5
	v_rcp_f32_e32 v6, v6
	v_rcp_f32_e32 v7, v7
	v_rcp_f32_e32 v8, v8
	v_rcp_f32_e32 v9, v9
	v_mov_b32_e32 v14, 0x48000
	v_lshl_add_u64 v[20:21], v[18:19], 0, v[14:15]
	v_pk_mul_f32 v[78:79], v[78:79], v[2:3]
	v_pk_mul_f32 v[80:81], v[80:81], v[4:5]
	v_pk_mul_f32 v[74:75], v[74:75], v[6:7]
	v_pk_mul_f32 v[76:77], v[76:77], v[8:9]
	v_pk_mul_f32 v[78:79], v[78:79], s[100:101] op_sel:[0,1]
	v_pk_mul_f32 v[80:81], v[80:81], s[100:101] op_sel:[0,1]
	v_pk_mul_f32 v[74:75], v[74:75], s[100:101] op_sel:[0,1]
	v_pk_mul_f32 v[76:77], v[76:77], s[100:101] op_sel:[0,1]
	v_cvt_pk_fp8_f32 v22, v78, v79
	v_cvt_pk_fp8_f32 v23, v74, v75
	v_cvt_pk_fp8_f32 v22, v80, v81 op_sel:[0,0,1]
	v_cvt_pk_fp8_f32 v23, v76, v77 op_sel:[0,0,1]
	global_store_dwordx2 v[20:21], v[22:23], off
	v_pk_fma_f32 v[62:63], v[62:63], s[98:99], v[224:225] op_sel_hi:[1,0,1]
	v_pk_fma_f32 v[64:65], v[64:65], s[98:99], v[226:227] op_sel_hi:[1,0,1]
	v_pk_fma_f32 v[58:59], v[58:59], s[98:99], v[228:229] op_sel_hi:[1,0,1]
	v_pk_fma_f32 v[60:61], v[60:61], s[98:99], v[230:231] op_sel_hi:[1,0,1]
	v_pk_fma_f32 v[54:55], v[54:55], s[98:99], v[232:233] op_sel_hi:[1,0,1]
	v_pk_fma_f32 v[56:57], v[56:57], s[98:99], v[234:235] op_sel_hi:[1,0,1]
	v_pk_fma_f32 v[50:51], v[50:51], s[98:99], v[236:237] op_sel_hi:[1,0,1]
	v_pk_fma_f32 v[52:53], v[52:53], s[98:99], v[238:239] op_sel_hi:[1,0,1]
	v_min_f32_e32 v62, 0x40e00000, v62
	v_min_f32_e32 v63, 0x40e00000, v63
	v_min_f32_e32 v64, 0x40e00000, v64
	v_min_f32_e32 v65, 0x40e00000, v65
	v_min_f32_e32 v58, 0x40e00000, v58
	v_min_f32_e32 v59, 0x40e00000, v59
	v_min_f32_e32 v60, 0x40e00000, v60
	v_min_f32_e32 v61, 0x40e00000, v61
	v_med3_f32 v54, v54, s59, v189
	v_med3_f32 v55, v55, s59, v189
	v_med3_f32 v56, v56, s59, v189
	v_med3_f32 v57, v57, s59, v189
	v_med3_f32 v50, v50, s59, v189
	v_med3_f32 v51, v51, s59, v189
	v_med3_f32 v52, v52, s59, v189
	v_med3_f32 v53, v53, s59, v189
	v_pk_mul_f32 v[2:3], v[62:63], s[98:99] op_sel:[0,1]
	v_pk_mul_f32 v[4:5], v[64:65], s[98:99] op_sel:[0,1]
	v_pk_mul_f32 v[6:7], v[58:59], s[98:99] op_sel:[0,1]
	v_pk_mul_f32 v[8:9], v[60:61], s[98:99] op_sel:[0,1]
	v_pk_mul_f32 v[2:3], v[2:3], s[100:101] op_sel_hi:[1,0]
	v_pk_mul_f32 v[4:5], v[4:5], s[100:101] op_sel_hi:[1,0]
	v_pk_mul_f32 v[6:7], v[6:7], s[100:101] op_sel_hi:[1,0]
	v_pk_mul_f32 v[8:9], v[8:9], s[100:101] op_sel_hi:[1,0]
	v_exp_f32_e32 v2, v2
	v_exp_f32_e32 v3, v3
	v_exp_f32_e32 v4, v4
	v_exp_f32_e32 v5, v5
	v_exp_f32_e32 v6, v6
	v_exp_f32_e32 v7, v7
	v_exp_f32_e32 v8, v8
	v_exp_f32_e32 v9, v9
	v_pk_add_f32 v[54:55], v[54:55], v[16:17]
	v_pk_add_f32 v[56:57], v[56:57], v[16:17]
	v_pk_add_f32 v[50:51], v[50:51], v[16:17]
	v_pk_add_f32 v[52:53], v[52:53], v[16:17]
	v_pk_add_f32 v[2:3], v[2:3], v[16:17]
	v_pk_add_f32 v[4:5], v[4:5], v[16:17]
	v_pk_add_f32 v[6:7], v[6:7], v[16:17]
	v_pk_add_f32 v[8:9], v[8:9], v[16:17]
	v_pk_mul_f32 v[62:63], v[62:63], v[54:55]
	v_pk_mul_f32 v[64:65], v[64:65], v[56:57]
	v_pk_mul_f32 v[58:59], v[58:59], v[50:51]
	v_pk_mul_f32 v[60:61], v[60:61], v[52:53]
	v_rcp_f32_e32 v2, v2
	v_rcp_f32_e32 v3, v3
	v_rcp_f32_e32 v4, v4
	v_rcp_f32_e32 v5, v5
	v_rcp_f32_e32 v6, v6
	v_rcp_f32_e32 v7, v7
	v_rcp_f32_e32 v8, v8
	v_rcp_f32_e32 v9, v9
	v_mov_b32_e32 v14, 0x50000
	v_lshl_add_u64 v[20:21], v[18:19], 0, v[14:15]
	v_pk_mul_f32 v[62:63], v[62:63], v[2:3]
	v_pk_mul_f32 v[64:65], v[64:65], v[4:5]
	v_pk_mul_f32 v[58:59], v[58:59], v[6:7]
	v_pk_mul_f32 v[60:61], v[60:61], v[8:9]
	v_pk_mul_f32 v[62:63], v[62:63], s[100:101] op_sel:[0,1]
	v_pk_mul_f32 v[64:65], v[64:65], s[100:101] op_sel:[0,1]
	v_pk_mul_f32 v[58:59], v[58:59], s[100:101] op_sel:[0,1]
	v_pk_mul_f32 v[60:61], v[60:61], s[100:101] op_sel:[0,1]
	v_cvt_pk_fp8_f32 v22, v62, v63
	v_cvt_pk_fp8_f32 v23, v58, v59
	v_cvt_pk_fp8_f32 v22, v64, v65 op_sel:[0,0,1]
	v_cvt_pk_fp8_f32 v23, v60, v61 op_sel:[0,0,1]
	global_store_dwordx2 v[20:21], v[22:23], off
	v_pk_fma_f32 v[46:47], v[46:47], s[98:99], v[224:225] op_sel_hi:[1,0,1]
	v_pk_fma_f32 v[48:49], v[48:49], s[98:99], v[226:227] op_sel_hi:[1,0,1]
	v_pk_fma_f32 v[42:43], v[42:43], s[98:99], v[228:229] op_sel_hi:[1,0,1]
	v_pk_fma_f32 v[44:45], v[44:45], s[98:99], v[230:231] op_sel_hi:[1,0,1]
	v_pk_fma_f32 v[38:39], v[38:39], s[98:99], v[232:233] op_sel_hi:[1,0,1]
	v_pk_fma_f32 v[40:41], v[40:41], s[98:99], v[234:235] op_sel_hi:[1,0,1]
	v_pk_fma_f32 v[34:35], v[34:35], s[98:99], v[236:237] op_sel_hi:[1,0,1]
	v_pk_fma_f32 v[36:37], v[36:37], s[98:99], v[238:239] op_sel_hi:[1,0,1]
	v_min_f32_e32 v46, 0x40e00000, v46
	v_min_f32_e32 v47, 0x40e00000, v47
	v_min_f32_e32 v48, 0x40e00000, v48
	v_min_f32_e32 v49, 0x40e00000, v49
	v_min_f32_e32 v42, 0x40e00000, v42
	v_min_f32_e32 v43, 0x40e00000, v43
	v_min_f32_e32 v44, 0x40e00000, v44
	v_min_f32_e32 v45, 0x40e00000, v45
	v_med3_f32 v38, v38, s59, v189
	v_med3_f32 v39, v39, s59, v189
	v_med3_f32 v40, v40, s59, v189
	v_med3_f32 v41, v41, s59, v189
	v_med3_f32 v34, v34, s59, v189
	v_med3_f32 v35, v35, s59, v189
	v_med3_f32 v36, v36, s59, v189
	v_med3_f32 v37, v37, s59, v189
	v_pk_mul_f32 v[2:3], v[46:47], s[98:99] op_sel:[0,1]
	v_pk_mul_f32 v[4:5], v[48:49], s[98:99] op_sel:[0,1]
	v_pk_mul_f32 v[6:7], v[42:43], s[98:99] op_sel:[0,1]
	v_pk_mul_f32 v[8:9], v[44:45], s[98:99] op_sel:[0,1]
	v_pk_mul_f32 v[2:3], v[2:3], s[100:101] op_sel_hi:[1,0]
	v_pk_mul_f32 v[4:5], v[4:5], s[100:101] op_sel_hi:[1,0]
	v_pk_mul_f32 v[6:7], v[6:7], s[100:101] op_sel_hi:[1,0]
	v_pk_mul_f32 v[8:9], v[8:9], s[100:101] op_sel_hi:[1,0]
	v_exp_f32_e32 v2, v2
	v_exp_f32_e32 v3, v3
	v_exp_f32_e32 v4, v4
	v_exp_f32_e32 v5, v5
	v_exp_f32_e32 v6, v6
	v_exp_f32_e32 v7, v7
	v_exp_f32_e32 v8, v8
	v_exp_f32_e32 v9, v9
	v_pk_add_f32 v[38:39], v[38:39], v[16:17]
	v_pk_add_f32 v[40:41], v[40:41], v[16:17]
	v_pk_add_f32 v[34:35], v[34:35], v[16:17]
	v_pk_add_f32 v[36:37], v[36:37], v[16:17]
	v_pk_add_f32 v[2:3], v[2:3], v[16:17]
	v_pk_add_f32 v[4:5], v[4:5], v[16:17]
	v_pk_add_f32 v[6:7], v[6:7], v[16:17]
	v_pk_add_f32 v[8:9], v[8:9], v[16:17]
	v_pk_mul_f32 v[46:47], v[46:47], v[38:39]
	v_pk_mul_f32 v[48:49], v[48:49], v[40:41]
	v_pk_mul_f32 v[42:43], v[42:43], v[34:35]
	v_pk_mul_f32 v[44:45], v[44:45], v[36:37]
	v_rcp_f32_e32 v2, v2
	v_rcp_f32_e32 v3, v3
	v_rcp_f32_e32 v4, v4
	v_rcp_f32_e32 v5, v5
	v_rcp_f32_e32 v6, v6
	v_rcp_f32_e32 v7, v7
	v_rcp_f32_e32 v8, v8
	v_rcp_f32_e32 v9, v9
	v_mov_b32_e32 v14, 0x58000
	v_lshl_add_u64 v[20:21], v[18:19], 0, v[14:15]
	v_pk_mul_f32 v[46:47], v[46:47], v[2:3]
	v_pk_mul_f32 v[48:49], v[48:49], v[4:5]
	v_pk_mul_f32 v[42:43], v[42:43], v[6:7]
	v_pk_mul_f32 v[44:45], v[44:45], v[8:9]
	v_pk_mul_f32 v[46:47], v[46:47], s[100:101] op_sel:[0,1]
	v_pk_mul_f32 v[48:49], v[48:49], s[100:101] op_sel:[0,1]
	v_pk_mul_f32 v[42:43], v[42:43], s[100:101] op_sel:[0,1]
	v_pk_mul_f32 v[44:45], v[44:45], s[100:101] op_sel:[0,1]
	v_cvt_pk_fp8_f32 v22, v46, v47
	v_cvt_pk_fp8_f32 v23, v42, v43
	v_cvt_pk_fp8_f32 v22, v48, v49 op_sel:[0,0,1]
	v_cvt_pk_fp8_f32 v23, v44, v45 op_sel:[0,0,1]
	s_andn2_b64 vcc, exec, s[4:5]
	s_mov_b64 s[4:5], -1
	global_store_dwordx2 v[20:21], v[22:23], off
	s_cbranch_vccnz .LBB0_1470
	s_andn2_b64 vcc, exec, s[12:13]
	s_cbranch_vccnz .LBB0_1469
	s_barrier
	s_branch .LBB0_1469
